# grid barrier: XCD-last workgroup issues its L1 invalidate behind the top-level arrival atomic and waits vmcnt(1) for the atomic only; invalidate overlaps the top-generation wait
# speedup vs baseline: 1.0056x; 1.0037x over previous
.LBB0_224:
	s_or_b64 exec, exec, s[10:11]
	buffer_inv sc1
	v_cvt_f32_u32_e32 v3, v0
	s_waitcnt vmcnt(1)
	v_readfirstlane_b32 s8, v2
	s_add_u32 s10, s84, 0x7500
	s_addc_u32 s11, s85, 0
	v_rcp_iflag_f32_e32 v3, v3
	v_add_u32_e32 v1, s8, v1
	v_add_u32_e32 v4, 1, v1
	s_mov_b64 s[12:13], -1
	v_mul_f32_e32 v2, 0x4f7ffffe, v3
	v_cvt_u32_f32_e32 v2, v2
	v_sub_u32_e32 v3, 0, v0
	v_mul_lo_u32 v3, v3, v2
	v_mul_hi_u32 v3, v2, v3
	v_add_u32_e32 v2, v2, v3
	v_mul_hi_u32 v2, v1, v2
	v_mul_lo_u32 v3, v2, v0
	v_sub_u32_e32 v1, v1, v3
	v_add_u32_e32 v5, 1, v2
	v_cmp_ge_u32_e32 vcc, v1, v0
	v_sub_u32_e32 v3, v1, v0
	s_nop 0
	v_cndmask_b32_e32 v2, v2, v5, vcc
	v_cndmask_b32_e32 v1, v1, v3, vcc
	v_add_u32_e32 v3, 1, v2
	v_cmp_ge_u32_e32 vcc, v1, v0
	s_nop 1
	v_cndmask_b32_e32 v2, v2, v3, vcc
	v_mul_lo_u32 v1, v0, v2
	v_add_u32_e32 v0, v1, v0
	v_cmp_ne_u32_e32 vcc, v4, v0
	v_mov_b64_e32 v[0:1], s[10:11]
	s_and_saveexec_b64 s[8:9], vcc
	s_cbranch_execz .LBB0_236
	v_mov_b32_e32 v0, 0
	global_load_dword v1, v0, s[10:11] sc1
	s_mov_b64 s[16:17], 0
	s_waitcnt vmcnt(0)
	v_cmp_eq_u32_e32 vcc, v1, v2
	s_and_saveexec_b64 s[14:15], vcc
	s_cbranch_execz .LBB0_235
	s_add_u32 s12, s84, 0x4200
	s_addc_u32 s13, s85, 0
	s_mov_b32 s26, 1
	s_branch .LBB0_228

.LBB0_238:
	s_or_b64 exec, exec, s[8:9]
	s_mov_b64 s[8:9], exec
	v_mbcnt_lo_u32_b32 v0, s8, 0
	v_mbcnt_hi_u32_b32 v0, s9, v0
	v_cmp_eq_u32_e32 vcc, 0, v0
	s_waitcnt vmcnt(0)
	s_and_saveexec_b64 s[10:11], vcc
	s_cbranch_execz .LBB0_240
	s_bcnt1_i32_b64 s8, s[8:9]
	v_mov_b32_e32 v0, 0x2000
	v_mov_b32_e32 v1, s8
	global_atomic_add v0, v1, s[6:7] offset:1024

.LBB0_312:
	s_or_b64 exec, exec, s[8:9]
	buffer_inv sc1
	s_waitcnt vmcnt(1)
	v_readfirstlane_b32 s6, v3
	v_sub_u32_e32 v4, 0, v2
	s_mov_b64 s[8:9], -1
	v_add_u32_e32 v3, s6, v0
	v_cvt_f32_u32_e32 v0, v2
	v_readlane_b32 s6, v254, 9
	v_readlane_b32 s7, v254, 10
	v_rcp_iflag_f32_e32 v0, v0
	s_nop 0
	v_mul_f32_e32 v0, 0x4f7ffffe, v0
	v_cvt_u32_f32_e32 v0, v0
	v_mul_lo_u32 v4, v4, v0
	v_mul_hi_u32 v4, v0, v4
	v_add_u32_e32 v0, v0, v4
	v_mul_hi_u32 v0, v3, v0
	v_mul_lo_u32 v4, v0, v2
	v_sub_u32_e32 v4, v3, v4
	v_cmp_ge_u32_e32 vcc, v4, v2
	v_add_u32_e32 v5, 1, v0
	v_add_u32_e32 v3, 1, v3
	v_cndmask_b32_e32 v0, v0, v5, vcc
	v_sub_u32_e32 v5, v4, v2
	v_cndmask_b32_e32 v4, v4, v5, vcc
	v_cmp_ge_u32_e32 vcc, v4, v2
	v_add_u32_e32 v4, 1, v0
	s_nop 0
	v_cndmask_b32_e32 v0, v0, v4, vcc
	v_mul_lo_u32 v4, v2, v0
	v_add_u32_e32 v2, v4, v2
	v_cmp_ne_u32_e32 vcc, v3, v2
	v_mov_b64_e32 v[2:3], s[6:7]
	s_and_saveexec_b64 s[6:7], vcc
	s_cbranch_execz .LBB0_324
	v_readlane_b32 s8, v254, 9
	v_readlane_b32 s9, v254, 10
	s_mov_b64 s[10:11], 0
	s_nop 3
	global_load_dword v2, v1, s[8:9] sc1
	s_waitcnt vmcnt(0)
	v_cmp_eq_u32_e32 vcc, v2, v0
	s_and_saveexec_b64 s[8:9], vcc
	s_cbranch_execz .LBB0_323
	s_mov_b32 s24, 1
	s_branch .LBB0_316

.LBB0_326:
	s_or_b64 exec, exec, s[6:7]
	s_mov_b64 s[6:7], exec
	v_mbcnt_lo_u32_b32 v0, s6, 0
	v_mbcnt_hi_u32_b32 v0, s7, v0
	v_cmp_eq_u32_e32 vcc, 0, v0
	s_waitcnt vmcnt(0)
	s_and_saveexec_b64 s[8:9], vcc
	s_cbranch_execz .LBB0_328
	s_bcnt1_i32_b64 s6, s[6:7]
	v_mov_b32_e32 v0, s6
	v_readlane_b32 s6, v254, 5
	v_readlane_b32 s7, v254, 6
	s_nop 4
	global_atomic_add v1, v0, s[6:7]

.LBB0_1590:
	s_or_b64 exec, exec, s[8:9]
	buffer_inv sc1
	s_waitcnt vmcnt(1)
	v_readfirstlane_b32 s6, v3
	v_sub_u32_e32 v4, 0, v2
	s_mov_b64 s[8:9], -1
	v_add_u32_e32 v3, s6, v0
	v_cvt_f32_u32_e32 v0, v2
	v_readlane_b32 s6, v254, 9
	v_readlane_b32 s7, v254, 10
	v_rcp_iflag_f32_e32 v0, v0
	s_nop 0
	v_mul_f32_e32 v0, 0x4f7ffffe, v0
	v_cvt_u32_f32_e32 v0, v0
	v_mul_lo_u32 v4, v4, v0
	v_mul_hi_u32 v4, v0, v4
	v_add_u32_e32 v0, v0, v4
	v_mul_hi_u32 v0, v3, v0
	v_mul_lo_u32 v4, v0, v2
	v_sub_u32_e32 v4, v3, v4
	v_cmp_ge_u32_e32 vcc, v4, v2
	v_add_u32_e32 v5, 1, v0
	v_add_u32_e32 v3, 1, v3
	v_cndmask_b32_e32 v0, v0, v5, vcc
	v_sub_u32_e32 v5, v4, v2
	v_cndmask_b32_e32 v4, v4, v5, vcc
	v_cmp_ge_u32_e32 vcc, v4, v2
	v_add_u32_e32 v4, 1, v0
	s_nop 0
	v_cndmask_b32_e32 v0, v0, v4, vcc
	v_mul_lo_u32 v4, v2, v0
	v_add_u32_e32 v2, v4, v2
	v_cmp_ne_u32_e32 vcc, v3, v2
	v_mov_b64_e32 v[2:3], s[6:7]
	s_and_saveexec_b64 s[6:7], vcc
	s_cbranch_execz .LBB0_1602
	v_readlane_b32 s8, v254, 9
	v_readlane_b32 s9, v254, 10
	s_mov_b64 s[10:11], 0
	s_nop 3
	global_load_dword v2, v1, s[8:9] sc1
	s_waitcnt vmcnt(0)
	v_cmp_eq_u32_e32 vcc, v2, v0
	s_and_saveexec_b64 s[8:9], vcc
	s_cbranch_execz .LBB0_1601
	s_mov_b32 s20, 1
	s_branch .LBB0_1594

.LBB0_1604:
	s_or_b64 exec, exec, s[6:7]
	s_mov_b64 s[6:7], exec
	v_mbcnt_lo_u32_b32 v0, s6, 0
	v_mbcnt_hi_u32_b32 v0, s7, v0
	v_cmp_eq_u32_e32 vcc, 0, v0
	s_waitcnt vmcnt(0)
	s_and_saveexec_b64 s[8:9], vcc
	s_cbranch_execnz .LBB0_1605
	s_getpc_b64 s[98:99]
